# speedup vs baseline: 1.0329x; 1.0033x over previous
.Lg1_noX:
	v_exp_f32_e32 v130, v106
	v_exp_f32_e32 v131, v107
	v_exp_f32_e32 v132, v108
	v_exp_f32_e32 v133, v109
	v_exp_f32_e32 v142, v70
	v_exp_f32_e32 v143, v71
	v_exp_f32_e32 v144, v72
	v_exp_f32_e32 v145, v73
	v_pk_add_f32 v[130:131], v[130:131], 1.0 op_sel_hi:[1,0]
	v_pk_add_f32 v[132:133], v[132:133], 1.0 op_sel_hi:[1,0]
	v_pk_add_f32 v[142:143], v[142:143], 1.0 op_sel_hi:[1,0]
	v_pk_add_f32 v[144:145], v[144:145], 1.0 op_sel_hi:[1,0]
	v_pk_mul_f32 v[134:135], v[130:131], v[132:133]
	v_pk_mul_f32 v[146:147], v[142:143], v[144:145]
	v_rcp_f32_e64 v136, -v134
	v_rcp_f32_e64 v137, -v135
	v_rcp_f32_e64 v148, -v146
	v_rcp_f32_e64 v149, -v147
	v_pk_add_f32 v[164:165], v[164:165], v[106:107]
	v_pk_add_f32 v[164:165], v[164:165], v[108:109]
	v_pk_mul_f32 v[162:163], v[162:163], v[134:135]
	v_pk_mul_f32 v[162:163], v[162:163], v[146:147]
	v_pk_add_f32 v[164:165], v[164:165], v[70:71]
	v_pk_add_f32 v[164:165], v[164:165], v[72:73]
	v_pk_mul_f32 v[140:141], v[136:137], v[130:131]
	v_pk_mul_f32 v[138:139], v[136:137], v[132:133]
	v_pk_mul_f32 v[152:153], v[148:149], v[142:143]
	v_pk_mul_f32 v[150:151], v[148:149], v[144:145]
	v_pk_fma_f32 v[138:139], v[138:139], 2.0, 1.0 op_sel_hi:[1,0,0]
	v_pk_fma_f32 v[140:141], v[140:141], 2.0, 1.0 op_sel_hi:[1,0,0]
	v_pk_fma_f32 v[150:151], v[150:151], 2.0, 1.0 op_sel_hi:[1,0,0]
	v_pk_fma_f32 v[152:153], v[152:153], 2.0, 1.0 op_sel_hi:[1,0,0]
	v_cvt_pk_bf16_f32 v158, v138, v139
	v_cvt_pk_bf16_f32 v159, v140, v141
	v_cvt_pk_bf16_f32 v160, v150, v151
	v_cvt_pk_bf16_f32 v161, v152, v153
	ds_read_b128 v[106:109], v172 offset:128
	ds_read_b128 v[70:73], v172 offset:192
	v_permlane16_swap_b32_e32 v158, v160
	v_permlane16_swap_b32_e32 v159, v161
	global_store_dwordx4 v228, v[158:161], s[58:59] offset:128 nt
	v_exp_f32_e32 v130, v90
	v_exp_f32_e32 v131, v91
	v_exp_f32_e32 v132, v92
	v_exp_f32_e32 v133, v93
	v_exp_f32_e32 v142, v42
	v_exp_f32_e32 v143, v43
	v_exp_f32_e32 v144, v44
	v_exp_f32_e32 v145, v45
	v_pk_add_f32 v[130:131], v[130:131], 1.0 op_sel_hi:[1,0]
	v_pk_add_f32 v[132:133], v[132:133], 1.0 op_sel_hi:[1,0]
	v_pk_add_f32 v[142:143], v[142:143], 1.0 op_sel_hi:[1,0]
	v_pk_add_f32 v[144:145], v[144:145], 1.0 op_sel_hi:[1,0]
	v_pk_mul_f32 v[134:135], v[130:131], v[132:133]
	v_pk_mul_f32 v[146:147], v[142:143], v[144:145]
	v_rcp_f32_e64 v136, -v134
	v_rcp_f32_e64 v137, -v135
	v_rcp_f32_e64 v148, -v146
	v_rcp_f32_e64 v149, -v147
	v_pk_add_f32 v[164:165], v[164:165], v[90:91]
	v_pk_add_f32 v[164:165], v[164:165], v[92:93]
	v_pk_mul_f32 v[174:175], v[134:135], v[146:147]
	v_pk_add_f32 v[164:165], v[164:165], v[42:43]
	v_pk_add_f32 v[164:165], v[164:165], v[44:45]
	v_pk_mul_f32 v[140:141], v[136:137], v[130:131]
	v_pk_mul_f32 v[138:139], v[136:137], v[132:133]
	v_pk_mul_f32 v[152:153], v[148:149], v[142:143]
	v_pk_mul_f32 v[150:151], v[148:149], v[144:145]
	v_pk_fma_f32 v[138:139], v[138:139], 2.0, 1.0 op_sel_hi:[1,0,0]
	v_pk_fma_f32 v[140:141], v[140:141], 2.0, 1.0 op_sel_hi:[1,0,0]
	v_pk_fma_f32 v[150:151], v[150:151], 2.0, 1.0 op_sel_hi:[1,0,0]
	v_pk_fma_f32 v[152:153], v[152:153], 2.0, 1.0 op_sel_hi:[1,0,0]
	v_cvt_pk_bf16_f32 v154, v138, v139
	v_cvt_pk_bf16_f32 v155, v140, v141
	v_cvt_pk_bf16_f32 v156, v150, v151
	v_cvt_pk_bf16_f32 v157, v152, v153
	ds_read_b128 v[90:93], v172 offset:512
	ds_read_b128 v[42:45], v172 offset:576
	v_permlane16_swap_b32_e32 v154, v156
	v_permlane16_swap_b32_e32 v155, v157
	global_store_dwordx4 v228, v[154:157], s[62:63] nt
	v_exp_f32_e32 v130, v126
	v_exp_f32_e32 v131, v127
	v_exp_f32_e32 v132, v128
	v_exp_f32_e32 v133, v129
	v_exp_f32_e32 v142, v58
	v_exp_f32_e32 v143, v59
	v_exp_f32_e32 v144, v60
	v_exp_f32_e32 v145, v61
	v_pk_add_f32 v[130:131], v[130:131], 1.0 op_sel_hi:[1,0]
	v_pk_add_f32 v[132:133], v[132:133], 1.0 op_sel_hi:[1,0]
	v_pk_add_f32 v[142:143], v[142:143], 1.0 op_sel_hi:[1,0]
	v_pk_add_f32 v[144:145], v[144:145], 1.0 op_sel_hi:[1,0]
	v_pk_mul_f32 v[134:135], v[130:131], v[132:133]
	v_pk_mul_f32 v[146:147], v[142:143], v[144:145]
	v_rcp_f32_e64 v136, -v134
	v_rcp_f32_e64 v137, -v135
	v_rcp_f32_e64 v148, -v146
	v_rcp_f32_e64 v149, -v147
	v_pk_add_f32 v[164:165], v[164:165], v[126:127]
	v_pk_add_f32 v[164:165], v[164:165], v[128:129]
	v_pk_mul_f32 v[174:175], v[174:175], v[134:135]
	v_pk_mul_f32 v[174:175], v[174:175], v[146:147]
	v_pk_add_f32 v[164:165], v[164:165], v[58:59]
	v_pk_add_f32 v[164:165], v[164:165], v[60:61]
	v_pk_mul_f32 v[140:141], v[136:137], v[130:131]
	v_pk_mul_f32 v[138:139], v[136:137], v[132:133]
	v_pk_mul_f32 v[152:153], v[148:149], v[142:143]
	v_pk_mul_f32 v[150:151], v[148:149], v[144:145]
	v_pk_fma_f32 v[138:139], v[138:139], 2.0, 1.0 op_sel_hi:[1,0,0]
	v_pk_fma_f32 v[140:141], v[140:141], 2.0, 1.0 op_sel_hi:[1,0,0]
	v_pk_fma_f32 v[150:151], v[150:151], 2.0, 1.0 op_sel_hi:[1,0,0]
	v_pk_fma_f32 v[152:153], v[152:153], 2.0, 1.0 op_sel_hi:[1,0,0]
	v_cvt_pk_bf16_f32 v158, v138, v139
	v_cvt_pk_bf16_f32 v159, v140, v141
	v_cvt_pk_bf16_f32 v160, v150, v151
	v_cvt_pk_bf16_f32 v161, v152, v153
	ds_read_b128 v[126:129], v172 offset:640
	ds_read_b128 v[58:61], v172 offset:704
	v_permlane16_swap_b32_e32 v158, v160
	v_permlane16_swap_b32_e32 v159, v161
	global_store_dwordx4 v228, v[158:161], s[62:63] offset:128 nt
	v_log_f32_e32 v166, v162
	v_log_f32_e32 v167, v163
	v_log_f32_e32 v170, v174
	v_log_f32_e32 v171, v175
	v_add_f32_e32 v168, v164, v165
	v_mul_f32_e32 v168, 0xbeb17218, v168
	v_add_f32_e32 v166, v166, v167
	v_add_f32_e32 v170, v170, v171
	v_add_f32_e32 v166, v166, v170
	v_add_f32_e32 v166, 0xc2000000, v166
	v_fmac_f32_e32 v168, 0x3f317218, v166
	v_mov_b32_e32 v169, v168
	s_nop 1
	v_permlane16_swap_b32_e32 v168, v169
	v_add_f32_e32 v168, v168, v169
	v_mov_b32_e32 v169, v168
	s_nop 1
	v_permlane32_swap_b32_e32 v168, v169
	v_add_f32_e32 v168, v168, v169
	s_mov_b64 exec, s[0:1]
	global_store_dword v229, v168, s[66:67]
	s_mov_b64 exec, -1
	v_exp_f32_e32 v130, v110
	v_exp_f32_e32 v131, v111
	v_exp_f32_e32 v132, v112
	v_exp_f32_e32 v133, v113
	v_exp_f32_e32 v142, v74
	v_exp_f32_e32 v143, v75
	v_exp_f32_e32 v144, v76
	v_exp_f32_e32 v145, v77
	v_pk_add_f32 v[130:131], v[130:131], 1.0 op_sel_hi:[1,0]
	v_pk_add_f32 v[132:133], v[132:133], 1.0 op_sel_hi:[1,0]
	v_pk_add_f32 v[142:143], v[142:143], 1.0 op_sel_hi:[1,0]
	v_pk_add_f32 v[144:145], v[144:145], 1.0 op_sel_hi:[1,0]
	v_pk_mul_f32 v[134:135], v[130:131], v[132:133]
	v_pk_mul_f32 v[146:147], v[142:143], v[144:145]
	v_rcp_f32_e64 v136, -v134
	v_rcp_f32_e64 v137, -v135
	v_rcp_f32_e64 v148, -v146
	v_rcp_f32_e64 v149, -v147
	v_pk_add_f32 v[164:165], v[110:111], v[112:113]
	v_pk_mul_f32 v[162:163], v[134:135], v[146:147]
	v_pk_add_f32 v[164:165], v[164:165], v[74:75]
	v_pk_add_f32 v[164:165], v[164:165], v[76:77]
	v_pk_mul_f32 v[140:141], v[136:137], v[130:131]
	v_pk_mul_f32 v[138:139], v[136:137], v[132:133]
	v_pk_mul_f32 v[152:153], v[148:149], v[142:143]
	v_pk_mul_f32 v[150:151], v[148:149], v[144:145]
	v_pk_fma_f32 v[138:139], v[138:139], 2.0, 1.0 op_sel_hi:[1,0,0]
	v_pk_fma_f32 v[140:141], v[140:141], 2.0, 1.0 op_sel_hi:[1,0,0]
	v_pk_fma_f32 v[150:151], v[150:151], 2.0, 1.0 op_sel_hi:[1,0,0]
	v_pk_fma_f32 v[152:153], v[152:153], 2.0, 1.0 op_sel_hi:[1,0,0]
	v_cvt_pk_bf16_f32 v154, v138, v139
	v_cvt_pk_bf16_f32 v155, v140, v141
	v_cvt_pk_bf16_f32 v156, v150, v151
	v_cvt_pk_bf16_f32 v157, v152, v153
	ds_read_b128 v[110:113], v172
	ds_read_b128 v[74:77], v172 offset:64
	v_permlane16_swap_b32_e32 v154, v156
	v_permlane16_swap_b32_e32 v155, v157
	global_store_dwordx4 v228, v[154:157], s[58:59] offset:2048 nt
	v_exp_f32_e32 v130, v102
	v_exp_f32_e32 v131, v103
	v_exp_f32_e32 v132, v104
	v_exp_f32_e32 v133, v105
	v_exp_f32_e32 v142, v66
	v_exp_f32_e32 v143, v67
	v_exp_f32_e32 v144, v68
	v_exp_f32_e32 v145, v69
	v_pk_add_f32 v[130:131], v[130:131], 1.0 op_sel_hi:[1,0]
	v_pk_add_f32 v[132:133], v[132:133], 1.0 op_sel_hi:[1,0]
	v_pk_add_f32 v[142:143], v[142:143], 1.0 op_sel_hi:[1,0]
	v_pk_add_f32 v[144:145], v[144:145], 1.0 op_sel_hi:[1,0]
	v_pk_mul_f32 v[134:135], v[130:131], v[132:133]
	v_pk_mul_f32 v[146:147], v[142:143], v[144:145]
	v_rcp_f32_e64 v136, -v134
	v_rcp_f32_e64 v137, -v135
	v_rcp_f32_e64 v148, -v146
	v_rcp_f32_e64 v149, -v147
	v_pk_add_f32 v[164:165], v[164:165], v[102:103]
	v_pk_add_f32 v[164:165], v[164:165], v[104:105]
	v_pk_mul_f32 v[162:163], v[162:163], v[134:135]
	v_pk_mul_f32 v[162:163], v[162:163], v[146:147]
	v_pk_add_f32 v[164:165], v[164:165], v[66:67]
	v_pk_add_f32 v[164:165], v[164:165], v[68:69]
	v_pk_mul_f32 v[140:141], v[136:137], v[130:131]
	v_pk_mul_f32 v[138:139], v[136:137], v[132:133]
	v_pk_mul_f32 v[152:153], v[148:149], v[142:143]
	v_pk_mul_f32 v[150:151], v[148:149], v[144:145]
	v_pk_fma_f32 v[138:139], v[138:139], 2.0, 1.0 op_sel_hi:[1,0,0]
	v_pk_fma_f32 v[140:141], v[140:141], 2.0, 1.0 op_sel_hi:[1,0,0]
	v_pk_fma_f32 v[150:151], v[150:151], 2.0, 1.0 op_sel_hi:[1,0,0]
	v_pk_fma_f32 v[152:153], v[152:153], 2.0, 1.0 op_sel_hi:[1,0,0]
	v_cvt_pk_bf16_f32 v158, v138, v139
	v_cvt_pk_bf16_f32 v159, v140, v141
	v_cvt_pk_bf16_f32 v160, v150, v151
	v_cvt_pk_bf16_f32 v161, v152, v153
	ds_read_b128 v[102:105], v172 offset:128
	ds_read_b128 v[66:69], v172 offset:192
	v_permlane16_swap_b32_e32 v158, v160
	v_permlane16_swap_b32_e32 v159, v161
	global_store_dwordx4 v228, v[158:161], s[58:59] offset:2176 nt
	v_exp_f32_e32 v130, v86
	v_exp_f32_e32 v131, v87
	v_exp_f32_e32 v132, v88
	v_exp_f32_e32 v133, v89
	v_exp_f32_e32 v142, v38
	v_exp_f32_e32 v143, v39
	v_exp_f32_e32 v144, v40
	v_exp_f32_e32 v145, v41
	v_pk_add_f32 v[130:131], v[130:131], 1.0 op_sel_hi:[1,0]
	v_pk_add_f32 v[132:133], v[132:133], 1.0 op_sel_hi:[1,0]
	v_pk_add_f32 v[142:143], v[142:143], 1.0 op_sel_hi:[1,0]
	v_pk_add_f32 v[144:145], v[144:145], 1.0 op_sel_hi:[1,0]
	v_pk_mul_f32 v[134:135], v[130:131], v[132:133]
	v_pk_mul_f32 v[146:147], v[142:143], v[144:145]
	v_rcp_f32_e64 v136, -v134
	v_rcp_f32_e64 v137, -v135
	v_rcp_f32_e64 v148, -v146
	v_rcp_f32_e64 v149, -v147
	v_pk_add_f32 v[164:165], v[164:165], v[86:87]
	v_pk_add_f32 v[164:165], v[164:165], v[88:89]
	v_pk_mul_f32 v[174:175], v[134:135], v[146:147]
	v_pk_add_f32 v[164:165], v[164:165], v[38:39]
	v_pk_add_f32 v[164:165], v[164:165], v[40:41]
	v_pk_mul_f32 v[140:141], v[136:137], v[130:131]
	v_pk_mul_f32 v[138:139], v[136:137], v[132:133]
	v_pk_mul_f32 v[152:153], v[148:149], v[142:143]
	v_pk_mul_f32 v[150:151], v[148:149], v[144:145]
	v_pk_fma_f32 v[138:139], v[138:139], 2.0, 1.0 op_sel_hi:[1,0,0]
	v_pk_fma_f32 v[140:141], v[140:141], 2.0, 1.0 op_sel_hi:[1,0,0]
	v_pk_fma_f32 v[150:151], v[150:151], 2.0, 1.0 op_sel_hi:[1,0,0]
	v_pk_fma_f32 v[152:153], v[152:153], 2.0, 1.0 op_sel_hi:[1,0,0]
	v_cvt_pk_bf16_f32 v154, v138, v139
	v_cvt_pk_bf16_f32 v155, v140, v141
	v_cvt_pk_bf16_f32 v156, v150, v151
	v_cvt_pk_bf16_f32 v157, v152, v153
	ds_read_b128 v[86:89], v172 offset:512
	ds_read_b128 v[38:41], v172 offset:576
	v_permlane16_swap_b32_e32 v154, v156
	v_permlane16_swap_b32_e32 v155, v157
	global_store_dwordx4 v228, v[154:157], s[62:63] offset:2048 nt
	v_exp_f32_e32 v130, v122
	v_exp_f32_e32 v131, v123
	v_exp_f32_e32 v132, v124
	v_exp_f32_e32 v133, v125
	v_exp_f32_e32 v142, v50
	v_exp_f32_e32 v143, v51
	v_exp_f32_e32 v144, v52
	v_exp_f32_e32 v145, v53
	v_pk_add_f32 v[130:131], v[130:131], 1.0 op_sel_hi:[1,0]
	v_pk_add_f32 v[132:133], v[132:133], 1.0 op_sel_hi:[1,0]
	v_pk_add_f32 v[142:143], v[142:143], 1.0 op_sel_hi:[1,0]
	v_pk_add_f32 v[144:145], v[144:145], 1.0 op_sel_hi:[1,0]
	v_pk_mul_f32 v[134:135], v[130:131], v[132:133]
	v_pk_mul_f32 v[146:147], v[142:143], v[144:145]
	v_rcp_f32_e64 v136, -v134
	v_rcp_f32_e64 v137, -v135
	v_rcp_f32_e64 v148, -v146
	v_rcp_f32_e64 v149, -v147
	v_pk_add_f32 v[164:165], v[164:165], v[122:123]
	v_pk_add_f32 v[164:165], v[164:165], v[124:125]
	v_pk_mul_f32 v[174:175], v[174:175], v[134:135]
	v_pk_mul_f32 v[174:175], v[174:175], v[146:147]
	v_pk_add_f32 v[164:165], v[164:165], v[50:51]
	v_pk_add_f32 v[164:165], v[164:165], v[52:53]
	v_pk_mul_f32 v[140:141], v[136:137], v[130:131]
	v_pk_mul_f32 v[138:139], v[136:137], v[132:133]
	v_pk_mul_f32 v[152:153], v[148:149], v[142:143]
	v_pk_mul_f32 v[150:151], v[148:149], v[144:145]
	v_pk_fma_f32 v[138:139], v[138:139], 2.0, 1.0 op_sel_hi:[1,0,0]
	v_pk_fma_f32 v[140:141], v[140:141], 2.0, 1.0 op_sel_hi:[1,0,0]
	v_pk_fma_f32 v[150:151], v[150:151], 2.0, 1.0 op_sel_hi:[1,0,0]
	v_pk_fma_f32 v[152:153], v[152:153], 2.0, 1.0 op_sel_hi:[1,0,0]
	v_cvt_pk_bf16_f32 v158, v138, v139
	v_cvt_pk_bf16_f32 v159, v140, v141
	v_cvt_pk_bf16_f32 v160, v150, v151
	v_cvt_pk_bf16_f32 v161, v152, v153
	ds_read_b128 v[122:125], v172 offset:640
	ds_read_b128 v[50:53], v172 offset:704
	v_permlane16_swap_b32_e32 v158, v160
	v_permlane16_swap_b32_e32 v159, v161
	global_store_dwordx4 v228, v[158:161], s[62:63] offset:2176 nt
	v_log_f32_e32 v166, v162
	v_log_f32_e32 v167, v163
	v_log_f32_e32 v170, v174
	v_log_f32_e32 v171, v175
	v_add_f32_e32 v168, v164, v165
	v_mul_f32_e32 v168, 0xbeb17218, v168
	v_add_f32_e32 v166, v166, v167
	v_add_f32_e32 v170, v170, v171
	v_add_f32_e32 v166, v166, v170
	v_add_f32_e32 v166, 0xc2000000, v166
	v_fmac_f32_e32 v168, 0x3f317218, v166
	v_mov_b32_e32 v169, v168
	s_nop 1
	v_permlane16_swap_b32_e32 v168, v169
	v_add_f32_e32 v168, v168, v169
	v_mov_b32_e32 v169, v168
	s_nop 1
	v_permlane32_swap_b32_e32 v168, v169
	v_add_f32_e32 v168, v168, v169
	s_mov_b64 exec, s[0:1]
	global_store_dword v229, v168, s[66:67] offset:64
	s_mov_b64 exec, -1
	v_exp_f32_e32 v130, v98
	v_exp_f32_e32 v131, v99
	v_exp_f32_e32 v132, v100
	v_exp_f32_e32 v133, v101
	v_exp_f32_e32 v142, v62
	v_exp_f32_e32 v143, v63
	v_exp_f32_e32 v144, v64
	v_exp_f32_e32 v145, v65
	v_pk_add_f32 v[130:131], v[130:131], 1.0 op_sel_hi:[1,0]
	v_pk_add_f32 v[132:133], v[132:133], 1.0 op_sel_hi:[1,0]
	v_pk_add_f32 v[142:143], v[142:143], 1.0 op_sel_hi:[1,0]
	v_pk_add_f32 v[144:145], v[144:145], 1.0 op_sel_hi:[1,0]
	v_pk_mul_f32 v[134:135], v[130:131], v[132:133]
	v_pk_mul_f32 v[146:147], v[142:143], v[144:145]
	v_rcp_f32_e64 v136, -v134
	v_rcp_f32_e64 v137, -v135
	v_rcp_f32_e64 v148, -v146
	v_rcp_f32_e64 v149, -v147
	v_pk_add_f32 v[164:165], v[98:99], v[100:101]
	v_pk_mul_f32 v[162:163], v[134:135], v[146:147]
	v_pk_add_f32 v[164:165], v[164:165], v[62:63]
	v_pk_add_f32 v[164:165], v[164:165], v[64:65]
	v_pk_mul_f32 v[140:141], v[136:137], v[130:131]
	v_pk_mul_f32 v[138:139], v[136:137], v[132:133]
	v_pk_mul_f32 v[152:153], v[148:149], v[142:143]
	v_pk_mul_f32 v[150:151], v[148:149], v[144:145]
	v_pk_fma_f32 v[138:139], v[138:139], 2.0, 1.0 op_sel_hi:[1,0,0]
	v_pk_fma_f32 v[140:141], v[140:141], 2.0, 1.0 op_sel_hi:[1,0,0]
	v_pk_fma_f32 v[150:151], v[150:151], 2.0, 1.0 op_sel_hi:[1,0,0]
	v_pk_fma_f32 v[152:153], v[152:153], 2.0, 1.0 op_sel_hi:[1,0,0]
	v_cvt_pk_bf16_f32 v154, v138, v139
	v_cvt_pk_bf16_f32 v155, v140, v141
	v_cvt_pk_bf16_f32 v156, v150, v151
	v_cvt_pk_bf16_f32 v157, v152, v153
	ds_read_b128 v[98:101], v172
	ds_read_b128 v[62:65], v172 offset:64
	v_permlane16_swap_b32_e32 v154, v156
	v_permlane16_swap_b32_e32 v155, v157
	global_store_dwordx4 v228, v[154:157], s[60:61] nt
	v_exp_f32_e32 v130, v94
	v_exp_f32_e32 v131, v95
	v_exp_f32_e32 v132, v96
	v_exp_f32_e32 v133, v97
	v_exp_f32_e32 v142, v54
	v_exp_f32_e32 v143, v55
	v_exp_f32_e32 v144, v56
	v_exp_f32_e32 v145, v57
	v_pk_add_f32 v[130:131], v[130:131], 1.0 op_sel_hi:[1,0]
	v_pk_add_f32 v[132:133], v[132:133], 1.0 op_sel_hi:[1,0]
	v_pk_add_f32 v[142:143], v[142:143], 1.0 op_sel_hi:[1,0]
	v_pk_add_f32 v[144:145], v[144:145], 1.0 op_sel_hi:[1,0]
	v_pk_mul_f32 v[134:135], v[130:131], v[132:133]
	v_pk_mul_f32 v[146:147], v[142:143], v[144:145]
	v_rcp_f32_e64 v136, -v134
	v_rcp_f32_e64 v137, -v135
	v_rcp_f32_e64 v148, -v146
	v_rcp_f32_e64 v149, -v147
	v_pk_add_f32 v[164:165], v[164:165], v[94:95]
	v_pk_add_f32 v[164:165], v[164:165], v[96:97]
	v_pk_mul_f32 v[162:163], v[162:163], v[134:135]
	v_pk_mul_f32 v[162:163], v[162:163], v[146:147]
	v_pk_add_f32 v[164:165], v[164:165], v[54:55]
	v_pk_add_f32 v[164:165], v[164:165], v[56:57]
	v_pk_mul_f32 v[140:141], v[136:137], v[130:131]
	v_pk_mul_f32 v[138:139], v[136:137], v[132:133]
	v_pk_mul_f32 v[152:153], v[148:149], v[142:143]
	v_pk_mul_f32 v[150:151], v[148:149], v[144:145]
	v_pk_fma_f32 v[138:139], v[138:139], 2.0, 1.0 op_sel_hi:[1,0,0]
	v_pk_fma_f32 v[140:141], v[140:141], 2.0, 1.0 op_sel_hi:[1,0,0]
	v_pk_fma_f32 v[150:151], v[150:151], 2.0, 1.0 op_sel_hi:[1,0,0]
	v_pk_fma_f32 v[152:153], v[152:153], 2.0, 1.0 op_sel_hi:[1,0,0]
	v_cvt_pk_bf16_f32 v158, v138, v139
	v_cvt_pk_bf16_f32 v159, v140, v141
	v_cvt_pk_bf16_f32 v160, v150, v151
	v_cvt_pk_bf16_f32 v161, v152, v153
	ds_read_b128 v[94:97], v172 offset:128
	ds_read_b128 v[54:57], v172 offset:192
	v_permlane16_swap_b32_e32 v158, v160
	v_permlane16_swap_b32_e32 v159, v161
	global_store_dwordx4 v228, v[158:161], s[60:61] offset:128 nt
	v_exp_f32_e32 v130, v82
	v_exp_f32_e32 v131, v83
	v_exp_f32_e32 v132, v84
	v_exp_f32_e32 v133, v85
	v_exp_f32_e32 v142, v34
	v_exp_f32_e32 v143, v35
	v_exp_f32_e32 v144, v36
	v_exp_f32_e32 v145, v37
	v_pk_add_f32 v[130:131], v[130:131], 1.0 op_sel_hi:[1,0]
	v_pk_add_f32 v[132:133], v[132:133], 1.0 op_sel_hi:[1,0]
	v_pk_add_f32 v[142:143], v[142:143], 1.0 op_sel_hi:[1,0]
	v_pk_add_f32 v[144:145], v[144:145], 1.0 op_sel_hi:[1,0]
	v_pk_mul_f32 v[134:135], v[130:131], v[132:133]
	v_pk_mul_f32 v[146:147], v[142:143], v[144:145]
	v_rcp_f32_e64 v136, -v134
	v_rcp_f32_e64 v137, -v135
	v_rcp_f32_e64 v148, -v146
	v_rcp_f32_e64 v149, -v147
	v_pk_add_f32 v[164:165], v[164:165], v[82:83]
	v_pk_add_f32 v[164:165], v[164:165], v[84:85]
	v_pk_mul_f32 v[174:175], v[134:135], v[146:147]
	v_pk_add_f32 v[164:165], v[164:165], v[34:35]
	v_pk_add_f32 v[164:165], v[164:165], v[36:37]
	v_pk_mul_f32 v[140:141], v[136:137], v[130:131]
	v_pk_mul_f32 v[138:139], v[136:137], v[132:133]
	v_pk_mul_f32 v[152:153], v[148:149], v[142:143]
	v_pk_mul_f32 v[150:151], v[148:149], v[144:145]
	v_pk_fma_f32 v[138:139], v[138:139], 2.0, 1.0 op_sel_hi:[1,0,0]
	v_pk_fma_f32 v[140:141], v[140:141], 2.0, 1.0 op_sel_hi:[1,0,0]
	v_pk_fma_f32 v[150:151], v[150:151], 2.0, 1.0 op_sel_hi:[1,0,0]
	v_pk_fma_f32 v[152:153], v[152:153], 2.0, 1.0 op_sel_hi:[1,0,0]
	v_cvt_pk_bf16_f32 v154, v138, v139
	v_cvt_pk_bf16_f32 v155, v140, v141
	v_cvt_pk_bf16_f32 v156, v150, v151
	v_cvt_pk_bf16_f32 v157, v152, v153
	ds_read_b128 v[82:85], v172 offset:512
	ds_read_b128 v[34:37], v172 offset:576
	v_permlane16_swap_b32_e32 v154, v156
	v_permlane16_swap_b32_e32 v155, v157
	global_store_dwordx4 v228, v[154:157], s[64:65] nt
	v_exp_f32_e32 v130, v118
	v_exp_f32_e32 v131, v119
	v_exp_f32_e32 v132, v120
	v_exp_f32_e32 v133, v121
	v_exp_f32_e32 v142, v46
	v_exp_f32_e32 v143, v47
	v_exp_f32_e32 v144, v48
	v_exp_f32_e32 v145, v49
	v_pk_add_f32 v[130:131], v[130:131], 1.0 op_sel_hi:[1,0]
	v_pk_add_f32 v[132:133], v[132:133], 1.0 op_sel_hi:[1,0]
	v_pk_add_f32 v[142:143], v[142:143], 1.0 op_sel_hi:[1,0]
	v_pk_add_f32 v[144:145], v[144:145], 1.0 op_sel_hi:[1,0]
	v_pk_mul_f32 v[134:135], v[130:131], v[132:133]
	v_pk_mul_f32 v[146:147], v[142:143], v[144:145]
	v_rcp_f32_e64 v136, -v134
	v_rcp_f32_e64 v137, -v135
	v_rcp_f32_e64 v148, -v146
	v_rcp_f32_e64 v149, -v147
	v_pk_add_f32 v[164:165], v[164:165], v[118:119]
	v_pk_add_f32 v[164:165], v[164:165], v[120:121]
	v_pk_mul_f32 v[174:175], v[174:175], v[134:135]
	v_pk_mul_f32 v[174:175], v[174:175], v[146:147]
	v_pk_add_f32 v[164:165], v[164:165], v[46:47]
	v_pk_add_f32 v[164:165], v[164:165], v[48:49]
	v_pk_mul_f32 v[140:141], v[136:137], v[130:131]
	v_pk_mul_f32 v[138:139], v[136:137], v[132:133]
	v_pk_mul_f32 v[152:153], v[148:149], v[142:143]
	v_pk_mul_f32 v[150:151], v[148:149], v[144:145]
	v_pk_fma_f32 v[138:139], v[138:139], 2.0, 1.0 op_sel_hi:[1,0,0]
	v_pk_fma_f32 v[140:141], v[140:141], 2.0, 1.0 op_sel_hi:[1,0,0]
	v_pk_fma_f32 v[150:151], v[150:151], 2.0, 1.0 op_sel_hi:[1,0,0]
	v_pk_fma_f32 v[152:153], v[152:153], 2.0, 1.0 op_sel_hi:[1,0,0]
	v_cvt_pk_bf16_f32 v158, v138, v139
	v_cvt_pk_bf16_f32 v159, v140, v141
	v_cvt_pk_bf16_f32 v160, v150, v151
	v_cvt_pk_bf16_f32 v161, v152, v153
	ds_read_b128 v[118:121], v172 offset:640
	ds_read_b128 v[46:49], v172 offset:704
	v_permlane16_swap_b32_e32 v158, v160
	v_permlane16_swap_b32_e32 v159, v161
	global_store_dwordx4 v228, v[158:161], s[64:65] offset:128 nt
	v_log_f32_e32 v166, v162
	v_log_f32_e32 v167, v163
	v_log_f32_e32 v170, v174
	v_log_f32_e32 v171, v175
	v_add_f32_e32 v168, v164, v165
	v_mul_f32_e32 v168, 0xbeb17218, v168
	v_add_f32_e32 v166, v166, v167
	v_add_f32_e32 v170, v170, v171
	v_add_f32_e32 v166, v166, v170
	v_add_f32_e32 v166, 0xc2000000, v166
	v_fmac_f32_e32 v168, 0x3f317218, v166
	v_mov_b32_e32 v169, v168
	s_nop 1
	v_permlane16_swap_b32_e32 v168, v169
	v_add_f32_e32 v168, v168, v169
	v_mov_b32_e32 v169, v168
	s_nop 1
	v_permlane32_swap_b32_e32 v168, v169
	v_add_f32_e32 v168, v168, v169
	s_mov_b64 exec, s[0:1]
	global_store_dword v229, v168, s[66:67] offset:512
	s_mov_b64 exec, -1
	s_bitcmp1_b32 s20, 12
	s_cbranch_scc0 .Lg1_noY
	s_barrier
.Lg1_noY:
	v_exp_f32_e32 v130, v18
	v_exp_f32_e32 v131, v19
	v_exp_f32_e32 v132, v20
	v_exp_f32_e32 v133, v21
	v_exp_f32_e32 v142, v2
	v_exp_f32_e32 v143, v3
	v_exp_f32_e32 v144, v4
	v_exp_f32_e32 v145, v5
	v_pk_add_f32 v[130:131], v[130:131], 1.0 op_sel_hi:[1,0]
	v_pk_add_f32 v[132:133], v[132:133], 1.0 op_sel_hi:[1,0]
	v_pk_add_f32 v[142:143], v[142:143], 1.0 op_sel_hi:[1,0]
	v_pk_add_f32 v[144:145], v[144:145], 1.0 op_sel_hi:[1,0]
	v_pk_mul_f32 v[134:135], v[130:131], v[132:133]
	v_pk_mul_f32 v[146:147], v[142:143], v[144:145]
	v_rcp_f32_e64 v136, -v134
	v_rcp_f32_e64 v137, -v135
	v_rcp_f32_e64 v148, -v146
	v_rcp_f32_e64 v149, -v147
	v_pk_add_f32 v[164:165], v[18:19], v[20:21]
	v_pk_mul_f32 v[162:163], v[134:135], v[146:147]
	v_pk_add_f32 v[164:165], v[164:165], v[2:3]
	v_pk_add_f32 v[164:165], v[164:165], v[4:5]
	v_pk_mul_f32 v[140:141], v[136:137], v[130:131]
	v_pk_mul_f32 v[138:139], v[136:137], v[132:133]
	v_pk_mul_f32 v[152:153], v[148:149], v[142:143]
	v_pk_mul_f32 v[150:151], v[148:149], v[144:145]
	v_pk_fma_f32 v[138:139], v[138:139], 2.0, 1.0 op_sel_hi:[1,0,0]
	v_pk_fma_f32 v[140:141], v[140:141], 2.0, 1.0 op_sel_hi:[1,0,0]
	v_pk_fma_f32 v[150:151], v[150:151], 2.0, 1.0 op_sel_hi:[1,0,0]
	v_pk_fma_f32 v[152:153], v[152:153], 2.0, 1.0 op_sel_hi:[1,0,0]
	v_cvt_pk_bf16_f32 v154, v138, v139
	v_cvt_pk_bf16_f32 v155, v140, v141
	v_cvt_pk_bf16_f32 v156, v150, v151
	v_cvt_pk_bf16_f32 v157, v152, v153
	ds_read_b128 v[18:21], v172
	ds_read_b128 v[2:5], v172 offset:64
	v_permlane16_swap_b32_e32 v154, v156
	v_permlane16_swap_b32_e32 v155, v157
	global_store_dwordx4 v228, v[154:157], s[60:61] offset:2048 nt
	v_exp_f32_e32 v130, v26
	v_exp_f32_e32 v131, v27
	v_exp_f32_e32 v132, v28
	v_exp_f32_e32 v133, v29
	v_exp_f32_e32 v142, v10
	v_exp_f32_e32 v143, v11
	v_exp_f32_e32 v144, v12
	v_exp_f32_e32 v145, v13
	v_pk_add_f32 v[130:131], v[130:131], 1.0 op_sel_hi:[1,0]
	v_pk_add_f32 v[132:133], v[132:133], 1.0 op_sel_hi:[1,0]
	v_pk_add_f32 v[142:143], v[142:143], 1.0 op_sel_hi:[1,0]
	v_pk_add_f32 v[144:145], v[144:145], 1.0 op_sel_hi:[1,0]
	v_pk_mul_f32 v[134:135], v[130:131], v[132:133]
	v_pk_mul_f32 v[146:147], v[142:143], v[144:145]
	v_rcp_f32_e64 v136, -v134
	v_rcp_f32_e64 v137, -v135
	v_rcp_f32_e64 v148, -v146
	v_rcp_f32_e64 v149, -v147
	v_pk_add_f32 v[164:165], v[164:165], v[26:27]
	v_pk_add_f32 v[164:165], v[164:165], v[28:29]
	v_pk_mul_f32 v[162:163], v[162:163], v[134:135]
	v_pk_mul_f32 v[162:163], v[162:163], v[146:147]
	v_pk_add_f32 v[164:165], v[164:165], v[10:11]
	v_pk_add_f32 v[164:165], v[164:165], v[12:13]
	v_pk_mul_f32 v[140:141], v[136:137], v[130:131]
	v_pk_mul_f32 v[138:139], v[136:137], v[132:133]
	v_pk_mul_f32 v[152:153], v[148:149], v[142:143]
	v_pk_mul_f32 v[150:151], v[148:149], v[144:145]
	v_pk_fma_f32 v[138:139], v[138:139], 2.0, 1.0 op_sel_hi:[1,0,0]
	v_pk_fma_f32 v[140:141], v[140:141], 2.0, 1.0 op_sel_hi:[1,0,0]
	v_pk_fma_f32 v[150:151], v[150:151], 2.0, 1.0 op_sel_hi:[1,0,0]
	v_pk_fma_f32 v[152:153], v[152:153], 2.0, 1.0 op_sel_hi:[1,0,0]
	v_cvt_pk_bf16_f32 v158, v138, v139
	v_cvt_pk_bf16_f32 v159, v140, v141
	v_cvt_pk_bf16_f32 v160, v150, v151
	v_cvt_pk_bf16_f32 v161, v152, v153
	ds_read_b128 v[26:29], v172 offset:128
	ds_read_b128 v[10:13], v172 offset:192
	v_permlane16_swap_b32_e32 v158, v160
	v_permlane16_swap_b32_e32 v159, v161
	global_store_dwordx4 v228, v[158:161], s[60:61] offset:2176 nt
	v_exp_f32_e32 v130, v22
	v_exp_f32_e32 v131, v23
	v_exp_f32_e32 v132, v24
	v_exp_f32_e32 v133, v25
	v_exp_f32_e32 v142, v6
	v_exp_f32_e32 v143, v7
	v_exp_f32_e32 v144, v8
	v_exp_f32_e32 v145, v9
	v_pk_add_f32 v[130:131], v[130:131], 1.0 op_sel_hi:[1,0]
	v_pk_add_f32 v[132:133], v[132:133], 1.0 op_sel_hi:[1,0]
	v_pk_add_f32 v[142:143], v[142:143], 1.0 op_sel_hi:[1,0]
	v_pk_add_f32 v[144:145], v[144:145], 1.0 op_sel_hi:[1,0]
	v_pk_mul_f32 v[134:135], v[130:131], v[132:133]
	v_pk_mul_f32 v[146:147], v[142:143], v[144:145]
	v_rcp_f32_e64 v136, -v134
	v_rcp_f32_e64 v137, -v135
	v_rcp_f32_e64 v148, -v146
	v_rcp_f32_e64 v149, -v147
	v_pk_add_f32 v[164:165], v[164:165], v[22:23]
	v_pk_add_f32 v[164:165], v[164:165], v[24:25]
	v_pk_mul_f32 v[174:175], v[134:135], v[146:147]
	v_pk_add_f32 v[164:165], v[164:165], v[6:7]
	v_pk_add_f32 v[164:165], v[164:165], v[8:9]
	v_pk_mul_f32 v[140:141], v[136:137], v[130:131]
	v_pk_mul_f32 v[138:139], v[136:137], v[132:133]
	v_pk_mul_f32 v[152:153], v[148:149], v[142:143]
	v_pk_mul_f32 v[150:151], v[148:149], v[144:145]
	v_pk_fma_f32 v[138:139], v[138:139], 2.0, 1.0 op_sel_hi:[1,0,0]
	v_pk_fma_f32 v[140:141], v[140:141], 2.0, 1.0 op_sel_hi:[1,0,0]
	v_pk_fma_f32 v[150:151], v[150:151], 2.0, 1.0 op_sel_hi:[1,0,0]
	v_pk_fma_f32 v[152:153], v[152:153], 2.0, 1.0 op_sel_hi:[1,0,0]
	v_cvt_pk_bf16_f32 v154, v138, v139
	v_cvt_pk_bf16_f32 v155, v140, v141
	v_cvt_pk_bf16_f32 v156, v150, v151
	v_cvt_pk_bf16_f32 v157, v152, v153
	ds_read_b128 v[22:25], v172 offset:512
	ds_read_b128 v[6:9], v172 offset:576
	v_permlane16_swap_b32_e32 v154, v156
	v_permlane16_swap_b32_e32 v155, v157
	global_store_dwordx4 v228, v[154:157], s[64:65] offset:2048 nt
	v_exp_f32_e32 v130, v30
	v_exp_f32_e32 v131, v31
	v_exp_f32_e32 v132, v32
	v_exp_f32_e32 v133, v33
	v_exp_f32_e32 v142, v14
	v_exp_f32_e32 v143, v15
	v_exp_f32_e32 v144, v16
	v_exp_f32_e32 v145, v17
	v_pk_add_f32 v[130:131], v[130:131], 1.0 op_sel_hi:[1,0]
	v_pk_add_f32 v[132:133], v[132:133], 1.0 op_sel_hi:[1,0]
	v_pk_add_f32 v[142:143], v[142:143], 1.0 op_sel_hi:[1,0]
	v_pk_add_f32 v[144:145], v[144:145], 1.0 op_sel_hi:[1,0]
	v_pk_mul_f32 v[134:135], v[130:131], v[132:133]
	v_pk_mul_f32 v[146:147], v[142:143], v[144:145]
	v_rcp_f32_e64 v136, -v134
	v_rcp_f32_e64 v137, -v135
	v_rcp_f32_e64 v148, -v146
	v_rcp_f32_e64 v149, -v147
	v_pk_add_f32 v[164:165], v[164:165], v[30:31]
	v_pk_add_f32 v[164:165], v[164:165], v[32:33]
	v_pk_mul_f32 v[174:175], v[174:175], v[134:135]
	v_pk_mul_f32 v[174:175], v[174:175], v[146:147]
	v_pk_add_f32 v[164:165], v[164:165], v[14:15]
	v_pk_add_f32 v[164:165], v[164:165], v[16:17]
	v_pk_mul_f32 v[140:141], v[136:137], v[130:131]
	v_pk_mul_f32 v[138:139], v[136:137], v[132:133]
	v_pk_mul_f32 v[152:153], v[148:149], v[142:143]
	v_pk_mul_f32 v[150:151], v[148:149], v[144:145]
	v_pk_fma_f32 v[138:139], v[138:139], 2.0, 1.0 op_sel_hi:[1,0,0]
	v_pk_fma_f32 v[140:141], v[140:141], 2.0, 1.0 op_sel_hi:[1,0,0]
	v_pk_fma_f32 v[150:151], v[150:151], 2.0, 1.0 op_sel_hi:[1,0,0]
	v_pk_fma_f32 v[152:153], v[152:153], 2.0, 1.0 op_sel_hi:[1,0,0]
	v_cvt_pk_bf16_f32 v158, v138, v139
	v_cvt_pk_bf16_f32 v159, v140, v141
	v_cvt_pk_bf16_f32 v160, v150, v151
	v_cvt_pk_bf16_f32 v161, v152, v153
	ds_read_b128 v[30:33], v172 offset:640
	ds_read_b128 v[14:17], v172 offset:704
	v_permlane16_swap_b32_e32 v158, v160
	v_permlane16_swap_b32_e32 v159, v161
	global_store_dwordx4 v228, v[158:161], s[64:65] offset:2176 nt
	v_log_f32_e32 v166, v162
	v_log_f32_e32 v167, v163
	v_log_f32_e32 v170, v174
	v_log_f32_e32 v171, v175
	v_add_f32_e32 v168, v164, v165
	v_mul_f32_e32 v168, 0xbeb17218, v168
	v_add_f32_e32 v166, v166, v167
	v_add_f32_e32 v170, v170, v171
	v_add_f32_e32 v166, v166, v170
	v_add_f32_e32 v166, 0xc2000000, v166
	v_fmac_f32_e32 v168, 0x3f317218, v166
	v_mov_b32_e32 v169, v168
	s_nop 1
	v_permlane16_swap_b32_e32 v168, v169
	v_add_f32_e32 v168, v168, v169
	v_mov_b32_e32 v169, v168
	s_nop 1
	v_permlane32_swap_b32_e32 v168, v169
	v_add_f32_e32 v168, v168, v169
	s_mov_b64 exec, s[0:1]
	global_store_dword v229, v168, s[66:67] offset:576
	s_mov_b64 exec, -1
	s_mov_b64 s[2:3], 0
	s_branch .LBB3_5

amdhsa.kernels:
  - .agpr_count:     0
    .args:
      - .actual_access:  read_only
        .address_space:  global
        .offset:         0
        .size:           8
        .value_kind:     global_buffer
      - .actual_access:  read_only
        .address_space:  global
        .offset:         8
        .size:           8
        .value_kind:     global_buffer
      - .actual_access:  read_only
        .address_space:  global
        .offset:         16
        .size:           8
        .value_kind:     global_buffer
      - .actual_access:  write_only
        .address_space:  global
        .offset:         24
        .size:           8
        .value_kind:     global_buffer
      - .actual_access:  write_only
        .address_space:  global
        .offset:         32
        .size:           8
        .value_kind:     global_buffer
      - .actual_access:  write_only
        .address_space:  global
        .offset:         40
        .size:           8
        .value_kind:     global_buffer
      - .actual_access:  write_only
        .address_space:  global
        .offset:         48
        .size:           8
        .value_kind:     global_buffer
      - .actual_access:  read_only
        .address_space:  global
        .offset:         56
        .size:           8
        .value_kind:     global_buffer
      - .actual_access:  read_only
        .address_space:  global
        .offset:         64
        .size:           8
        .value_kind:     global_buffer
      - .actual_access:  write_only
        .address_space:  global
        .offset:         72
        .size:           8
        .value_kind:     global_buffer
    .group_segment_fixed_size: 8448
    .kernarg_segment_align: 8
    .kernarg_segment_size: 80
    .language:       OpenCL C
    .language_version:
      - 2
      - 0
    .max_flat_workgroup_size: 256
    .name:           _Z6prep_kPKfS0_S0_PDF16_S1_S1_S1_S1_S0_Pf
    .private_segment_fixed_size: 0
    .sgpr_count:     22
    .sgpr_spill_count: 0
    .symbol:         _Z6prep_kPKfS0_S0_PDF16_S1_S1_S1_S1_S0_Pf.kd
    .uniform_work_group_size: 1
    .uses_dynamic_stack: false
    .vgpr_count:     34
    .vgpr_spill_count: 0
    .wavefront_size: 64
  - .agpr_count:     0
    .args:
      - .actual_access:  read_only
        .address_space:  global
        .offset:         0
        .size:           8
        .value_kind:     global_buffer
      - .actual_access:  write_only
        .address_space:  global
        .offset:         8
        .size:           8
        .value_kind:     global_buffer
      - .actual_access:  read_only
        .address_space:  global
        .offset:         16
        .size:           8
        .value_kind:     global_buffer
      - .actual_access:  write_only
        .address_space:  global
        .offset:         24
        .size:           8
        .value_kind:     global_buffer
      - .offset:         32
        .size:           4
        .value_kind:     hidden_block_count_x
      - .offset:         36
        .size:           4
        .value_kind:     hidden_block_count_y
      - .offset:         40
        .size:           4
        .value_kind:     hidden_block_count_z
      - .offset:         44
        .size:           2
        .value_kind:     hidden_group_size_x
      - .offset:         46
        .size:           2
        .value_kind:     hidden_group_size_y
      - .offset:         48
        .size:           2
        .value_kind:     hidden_group_size_z
      - .offset:         50
        .size:           2
        .value_kind:     hidden_remainder_x
      - .offset:         52
        .size:           2
        .value_kind:     hidden_remainder_y
      - .offset:         54
        .size:           2
        .value_kind:     hidden_remainder_z
      - .offset:         72
        .size:           8
        .value_kind:     hidden_global_offset_x
      - .offset:         80
        .size:           8
        .value_kind:     hidden_global_offset_y
      - .offset:         88
        .size:           8
        .value_kind:     hidden_global_offset_z
      - .offset:         96
        .size:           2
        .value_kind:     hidden_grid_dims
    .group_segment_fixed_size: 0
    .kernarg_segment_align: 8
    .kernarg_segment_size: 288
    .language:       OpenCL C
    .language_version:
      - 2
      - 0
    .max_flat_workgroup_size: 1024
    .name:           _Z6post_kPKfPfPKDF16_PDF16_
    .private_segment_fixed_size: 0
    .sgpr_count:     14
    .sgpr_spill_count: 0
    .symbol:         _Z6post_kPKfPfPKDF16_PDF16_.kd
    .uniform_work_group_size: 1
    .uses_dynamic_stack: false
    .vgpr_count:     49
    .vgpr_spill_count: 0
    .wavefront_size: 64
  - .agpr_count:     0
    .args:
      - .actual_access:  read_only
        .address_space:  global
        .offset:         0
        .size:           8
        .value_kind:     global_buffer
      - .actual_access:  read_only
        .address_space:  global
        .offset:         8
        .size:           8
        .value_kind:     global_buffer
      - .actual_access:  write_only
        .address_space:  global
        .offset:         16
        .size:           8
        .value_kind:     global_buffer
      - .offset:         24
        .size:           4
        .value_kind:     hidden_block_count_x
      - .offset:         28
        .size:           4
        .value_kind:     hidden_block_count_y
      - .offset:         32
        .size:           4
        .value_kind:     hidden_block_count_z
      - .offset:         36
        .size:           2
        .value_kind:     hidden_group_size_x
      - .offset:         38
        .size:           2
        .value_kind:     hidden_group_size_y
      - .offset:         40
        .size:           2
        .value_kind:     hidden_group_size_z
      - .offset:         42
        .size:           2
        .value_kind:     hidden_remainder_x
      - .offset:         44
        .size:           2
        .value_kind:     hidden_remainder_y
      - .offset:         46
        .size:           2
        .value_kind:     hidden_remainder_z
      - .offset:         64
        .size:           8
        .value_kind:     hidden_global_offset_x
      - .offset:         72
        .size:           8
        .value_kind:     hidden_global_offset_y
      - .offset:         80
        .size:           8
        .value_kind:     hidden_global_offset_z
      - .offset:         88
        .size:           2
        .value_kind:     hidden_grid_dims
    .group_segment_fixed_size: 0
    .kernarg_segment_align: 8
    .kernarg_segment_size: 280
    .language:       OpenCL C
    .language_version:
      - 2
      - 0
    .max_flat_workgroup_size: 1024
    .name:           _Z8reduce_kPKDF16_PKfPf
    .private_segment_fixed_size: 0
    .sgpr_count:     16
    .sgpr_spill_count: 0
    .symbol:         _Z8reduce_kPKDF16_PKfPf.kd
    .uniform_work_group_size: 1
    .uses_dynamic_stack: false
    .vgpr_count:     42
    .vgpr_spill_count: 0
    .wavefront_size: 64
  - .agpr_count:     0
    .args:
      - .actual_access:  read_only
        .address_space:  global
        .offset:         0
        .size:           8
        .value_kind:     global_buffer
      - .actual_access:  read_only
        .address_space:  global
        .offset:         8
        .size:           8
        .value_kind:     global_buffer
      - .actual_access:  write_only
        .address_space:  global
        .offset:         16
        .size:           8
        .value_kind:     global_buffer
      - .address_space:  global
        .offset:         24
        .size:           8
        .value_kind:     global_buffer
      - .actual_access:  write_only
        .address_space:  global
        .offset:         32
        .size:           8
        .value_kind:     global_buffer
      - .actual_access:  read_only
        .address_space:  global
        .offset:         40
        .size:           8
        .value_kind:     global_buffer
      - .actual_access:  write_only
        .address_space:  global
        .offset:         48
        .size:           8
        .value_kind:     global_buffer
    .group_segment_fixed_size: 0
    .kernarg_segment_align: 8
    .kernarg_segment_size: 56
    .language:       OpenCL C
    .language_version:
      - 2
      - 0
    .max_flat_workgroup_size: 512
    .name:           _Z7gemm1_kPKDF16_S0_PDF16_PKfPfS0_S1_
    .private_segment_fixed_size: 0
    .sgpr_count:     74
    .sgpr_spill_count: 0
    .symbol:         _Z7gemm1_kPKDF16_S0_PDF16_PKfPfS0_S1_.kd
    .uniform_work_group_size: 1
    .uses_dynamic_stack: false
    .vgpr_count:     232
    .vgpr_spill_count: 0
    .wavefront_size: 64
  - .agpr_count:     0
    .args:
      - .actual_access:  read_only
        .address_space:  global
        .offset:         0
        .size:           8
        .value_kind:     global_buffer
      - .actual_access:  read_only
        .address_space:  global
        .offset:         8
        .size:           8
        .value_kind:     global_buffer
      - .offset:         16
        .size:           4
        .value_kind:     by_value
      - .offset:         20
        .size:           4
        .value_kind:     by_value
      - .offset:         24
        .size:           4
        .value_kind:     by_value
      - .offset:         28
        .size:           4
        .value_kind:     by_value
      - .actual_access:  read_only
        .address_space:  global
        .offset:         32
        .size:           8
        .value_kind:     global_buffer
      - .actual_access:  write_only
        .address_space:  global
        .offset:         40
        .size:           8
        .value_kind:     global_buffer
      - .actual_access:  read_only
        .address_space:  global
        .offset:         48
        .size:           8
        .value_kind:     global_buffer
      - .actual_access:  read_only
        .address_space:  global
        .offset:         56
        .size:           8
        .value_kind:     global_buffer
    .group_segment_fixed_size: 0
    .kernarg_segment_align: 8
    .kernarg_segment_size: 64
    .language:       OpenCL C
    .language_version:
      - 2
      - 0
    .max_flat_workgroup_size: 512
    .name:           _Z6gemm_kILi2EEvPKDF16_S1_iiiiPfPDF16_PKfS2_
    .private_segment_fixed_size: 0
    .sgpr_count:     70
    .sgpr_spill_count: 0
    .symbol:         _Z6gemm_kILi2EEvPKDF16_S1_iiiiPfPDF16_PKfS2_.kd
    .uniform_work_group_size: 1
    .uses_dynamic_stack: false
    .vgpr_count:     224
    .vgpr_spill_count: 0
    .wavefront_size: 64
  - .agpr_count:     0
    .args:
      - .actual_access:  read_only
        .address_space:  global
        .offset:         0
        .size:           8
        .value_kind:     global_buffer
      - .actual_access:  read_only
        .address_space:  global
        .offset:         8
        .size:           8
        .value_kind:     global_buffer
      - .offset:         16
        .size:           4
        .value_kind:     by_value
      - .offset:         20
        .size:           4
        .value_kind:     by_value
      - .offset:         24
        .size:           4
        .value_kind:     by_value
      - .offset:         28
        .size:           4
        .value_kind:     by_value
      - .actual_access:  read_only
        .address_space:  global
        .offset:         32
        .size:           8
        .value_kind:     global_buffer
      - .actual_access:  write_only
        .address_space:  global
        .offset:         40
        .size:           8
        .value_kind:     global_buffer
      - .actual_access:  read_only
        .address_space:  global
        .offset:         48
        .size:           8
        .value_kind:     global_buffer
      - .actual_access:  read_only
        .address_space:  global
        .offset:         56
        .size:           8
        .value_kind:     global_buffer
    .group_segment_fixed_size: 0
    .kernarg_segment_align: 8
    .kernarg_segment_size: 64
    .language:       OpenCL C
    .language_version:
      - 2
      - 0
    .max_flat_workgroup_size: 512
    .name:           _Z6gemm_kILi3EEvPKDF16_S1_iiiiPfPDF16_PKfS2_
    .private_segment_fixed_size: 0
    .sgpr_count:     51
    .sgpr_spill_count: 0
    .symbol:         _Z6gemm_kILi3EEvPKDF16_S1_iiiiPfPDF16_PKfS2_.kd
    .uniform_work_group_size: 1
    .uses_dynamic_stack: false
    .vgpr_count:     220
    .vgpr_spill_count: 0
    .wavefront_size: 64
